# epilogue row-scale loads hoisted (P10,P11) + 16B code placement shift at P10
# speedup vs baseline: 1.0118x; 1.0008x over previous
; #define LAS __attribute__((address_space(3)))
; #define LANE_TID() const int lane = lane_id(), tid = wave * 64 + lane
; __device__ __forceinline__ void moe_tables(const unsigned* cnt, LAS int* ts, const int tid) {
;     if (tid < NE) ts[64 + tid] = (int)__hip_atomic_load(cnt + tid, RLX_AGENT);
;     __syncthreads();
; __global__ void __launch_bounds__(512, 2) fwd_kernel(Params p) {
;     ...
;     if (IN(10)) { LANE_TID();
;         moe_tables(ctl + CW_CNT, ts, tid);
.LBB0_1046:
	s_or_b64 exec, exec, s[4:5]
	s_waitcnt lgkmcnt(0)
	s_barrier
	s_nop 0
	s_nop 0
	s_nop 0
	s_nop 0
	v_mbcnt_lo_u32_b32 v0, -1, 0
	v_mbcnt_hi_u32_b32 v0, -1, v0
	v_readlane_b32 s0, v252, 3
	s_nop 1
	v_add_u32_e32 v0, s0, v0
	v_cmp_gt_i32_e32 vcc, 32, v0
	s_and_saveexec_b64 s[4:5], vcc
	s_cbranch_execz .LBB0_1048
	v_ashrrev_i32_e32 v1, 31, v0
	v_lshl_add_u64 v[2:3], v[0:1], 2, s[20:21]
	global_load_dword v1, v[2:3], off sc1
	s_add_i32 s0, 0, 0x25100
	v_lshl_add_u32 v2, v0, 2, s0
	s_waitcnt vmcnt(0)
	ds_write_b32 v2, v1 offset:256
